# stream: wave-row rotation keyed on the hardware XCC id (s_getreg) instead of blockIdx&7, so every CU of one XCD is guaranteed the same stack phase; rest as v40
# baseline (speedup 1.0000x reference)
.LBB1_2:
	s_or_b64 exec, exec, s[0:1]
	s_lshr_b32 s8, s3, 6
	s_getreg_b32 s11, hwreg(HW_REG_XCC_ID, 0, 4)
	s_lshr_b32 s12, s2, 3
	s_and_b32 s12, s12, 1
	s_lshl_b32 s12, s12, 3
	s_add_i32 s8, s8, s11
	s_add_i32 s8, s8, s12
	s_and_b32 s8, s8, 15
	s_lshl_b32 s0, s2, 7
	v_and_b32_e32 v24, 63, v0
	s_add_i32 s9, s8, s0
	s_waitcnt lgkmcnt(0)
	s_and_b32 s1, s5, 0xffff
	s_mov_b32 s3, 0x20000
	s_brev_b32 s2, 16
	s_mov_b32 s0, s4
	v_lshlrev_b32_e32 v25, 4, v24
	s_lshl_b32 s4, s9, 12
	buffer_load_dwordx4 v[26:29], v25, s[0:3], s4 offen offset:1024 nt
	buffer_load_dwordx4 v[30:33], v25, s[0:3], s4 offen nt
	buffer_load_dwordx4 v[34:37], v25, s[0:3], s4 offen offset:2048 nt
	s_barrier
	s_add_i32 s5, s4, 0x10000
	buffer_load_dwordx4 v[38:41], v25, s[0:3], s5 offen offset:1024 nt
	buffer_load_dwordx4 v[42:45], v25, s[0:3], s5 offen nt
	buffer_load_dwordx4 v[16:19], v25, s[0:3], s4 offen offset:3072 nt
	s_add_i32 s10, s4, 0x20000
	buffer_load_dwordx4 v[46:49], v25, s[0:3], s5 offen offset:2048 nt
	buffer_load_dwordx4 v[20:23], v25, s[0:3], s5 offen offset:3072 nt
	buffer_load_dwordx4 v[50:53], v25, s[0:3], s10 offen offset:1024 nt
	buffer_load_dwordx4 v[54:57], v25, s[0:3], s10 offen nt
	ds_read_b128 v[4:7], v25 offset:1024
	ds_read_b128 v[0:3], v25
	ds_read_b128 v[12:15], v25 offset:2048
	ds_read_b128 v[8:11], v25 offset:3072
	s_add_i32 s5, s4, 0x30000
	v_cmp_gt_u32_e32 vcc, 8, v24
	s_waitcnt vmcnt(9) lgkmcnt(3)
	v_pk_mul_f32 v[28:29], v[6:7], v[28:29]
	v_pk_mul_f32 v[26:27], v[4:5], v[26:27]
	s_waitcnt vmcnt(8) lgkmcnt(2)
	v_pk_fma_f32 v[32:33], v[2:3], v[32:33], v[28:29]
	v_pk_fma_f32 v[30:31], v[0:1], v[30:31], v[26:27]
	buffer_load_dwordx4 v[26:29], v25, s[0:3], s5 offen offset:1024 nt
	s_waitcnt vmcnt(8) lgkmcnt(1)
	v_pk_fma_f32 v[58:59], v[14:15], v[36:37], v[32:33]
	v_pk_fma_f32 v[60:61], v[12:13], v[34:35], v[30:31]
	buffer_load_dwordx4 v[30:33], v25, s[0:3], s5 offen nt
	s_waitcnt vmcnt(8)
	v_pk_mul_f32 v[34:35], v[6:7], v[40:41]
	v_pk_mul_f32 v[36:37], v[4:5], v[38:39]
	s_waitcnt vmcnt(7)
	v_pk_fma_f32 v[44:45], v[2:3], v[44:45], v[34:35]
	v_pk_fma_f32 v[42:43], v[0:1], v[42:43], v[36:37]
	buffer_load_dwordx4 v[34:37], v25, s[0:3], s10 offen offset:2048 nt
	s_waitcnt vmcnt(4)
	v_pk_mul_f32 v[38:39], v[6:7], v[52:53]
	v_pk_mul_f32 v[40:41], v[4:5], v[50:51]
	s_waitcnt vmcnt(3)
	v_pk_fma_f32 v[50:51], v[2:3], v[56:57], v[38:39]
	v_pk_fma_f32 v[52:53], v[0:1], v[54:55], v[40:41]
	buffer_load_dwordx4 v[38:41], v25, s[0:3], s10 offen offset:3072 nt
	v_pk_fma_f32 v[48:49], v[14:15], v[48:49], v[44:45]
	v_pk_fma_f32 v[46:47], v[12:13], v[46:47], v[42:43]
	s_waitcnt lgkmcnt(0)
	v_pk_fma_f32 v[18:19], v[10:11], v[18:19], v[58:59]
	v_pk_fma_f32 v[16:17], v[8:9], v[16:17], v[60:61]
	v_add_f32_e32 v61, v18, v19
	v_add_f32_e32 v60, v16, v17
	v_pk_fma_f32 v[16:17], v[10:11], v[22:23], v[48:49]
	v_pk_fma_f32 v[18:19], v[8:9], v[20:21], v[46:47]
	v_add_f32_e32 v16, v16, v17
	v_add_f32_e32 v18, v18, v19
	v_add_f32_e32 v60, v60, v61
	v_add_f32_e32 v16, v18, v16
	s_add_i32 s10, s4, 0x50000
	s_waitcnt vmcnt(3)
	v_pk_mul_f32 v[28:29], v[6:7], v[28:29]
	v_pk_mul_f32 v[26:27], v[4:5], v[26:27]
	v_add_f32_dpp v16, v16, v16 quad_perm:[1,0,3,2] row_mask:0xf bank_mask:0xf bound_ctrl:1
	s_waitcnt vmcnt(2)
	v_pk_fma_f32 v[54:55], v[2:3], v[32:33], v[28:29]
	v_pk_fma_f32 v[56:57], v[0:1], v[30:31], v[26:27]
	buffer_load_dwordx4 v[26:29], v25, s[0:3], s5 offen offset:2048 nt
	buffer_load_dwordx4 v[30:33], v25, s[0:3], s5 offen offset:3072 nt
	s_add_i32 s5, s4, 0x40000
	buffer_load_dwordx4 v[42:45], v25, s[0:3], s5 offen offset:1024 nt
	s_waitcnt vmcnt(4)
	v_pk_fma_f32 v[50:51], v[14:15], v[36:37], v[50:51]
	v_pk_fma_f32 v[52:53], v[12:13], v[34:35], v[52:53]
	buffer_load_dwordx4 v[34:37], v25, s[0:3], s5 offen nt
	v_add_f32_dpp v16, v16, v16 quad_perm:[2,3,0,1] row_mask:0xf bank_mask:0xf bound_ctrl:1
	s_waitcnt vmcnt(4)
	v_pk_fma_f32 v[58:59], v[10:11], v[40:41], v[50:51]
	v_pk_fma_f32 v[38:39], v[8:9], v[38:39], v[52:53]
	v_add_f32_e32 v19, v58, v59
	v_add_f32_e32 v17, v38, v39
	v_add_f32_dpp v58, v60, v60 quad_perm:[1,0,3,2] row_mask:0xf bank_mask:0xf bound_ctrl:1
	v_add_f32_e32 v18, v17, v19
	v_add_f32_dpp v16, v16, v16 row_ror:4 row_mask:0xf bank_mask:0xf bound_ctrl:1
	v_add_f32_dpp v17, v58, v58 quad_perm:[2,3,0,1] row_mask:0xf bank_mask:0xf bound_ctrl:1
	buffer_load_dwordx4 v[20:23], v25, s[0:3], s5 offen offset:2048 nt
	buffer_load_dwordx4 v[46:49], v25, s[0:3], s5 offen offset:3072 nt
	v_add_f32_dpp v17, v17, v17 row_ror:4 row_mask:0xf bank_mask:0xf bound_ctrl:1
	v_add_f32_dpp v58, v16, v16 row_ror:8 row_mask:0xf bank_mask:0xf bound_ctrl:1
	buffer_load_dwordx4 v[38:41], v25, s[0:3], s10 offen nt
	buffer_load_dwordx4 v[50:53], v25, s[0:3], s10 offen offset:1024 nt
	v_add_f32_dpp v17, v17, v17 row_ror:8 row_mask:0xf bank_mask:0xf bound_ctrl:1
	v_mov_b32_e32 v19, v17
	v_mov_b32_e32 v59, v58
	s_nop 0
	v_permlane16_swap_b32_e32 v17, v19
	v_permlane16_swap_b32_e32 v58, v59
	v_add_f32_e32 v16, v17, v19
	v_add_f32_e32 v17, v58, v59
	s_add_i32 s5, s4, 0x60000
	s_add_i32 s4, s4, 0x70000
	v_add_f32_dpp v18, v18, v18 quad_perm:[1,0,3,2] row_mask:0xf bank_mask:0xf bound_ctrl:1
	s_waitcnt vmcnt(7)
	v_pk_fma_f32 v[28:29], v[14:15], v[28:29], v[54:55]
	v_pk_fma_f32 v[54:55], v[12:13], v[26:27], v[56:57]
	s_waitcnt vmcnt(6)
	v_pk_fma_f32 v[58:59], v[10:11], v[32:33], v[28:29]
	buffer_load_dwordx4 v[26:29], v25, s[0:3], s10 offen offset:2048 nt
	v_pk_fma_f32 v[54:55], v[8:9], v[30:31], v[54:55]
	buffer_load_dwordx4 v[30:33], v25, s[0:3], s10 offen offset:3072 nt
	v_add_f32_e32 v66, v54, v55
	s_waitcnt vmcnt(7)
	v_pk_mul_f32 v[54:55], v[6:7], v[44:45]
	v_pk_mul_f32 v[56:57], v[4:5], v[42:43]
	buffer_load_dwordx4 v[42:45], v25, s[0:3], s5 offen offset:1024 nt
	s_waitcnt vmcnt(7)
	v_pk_fma_f32 v[54:55], v[2:3], v[36:37], v[54:55]
	v_pk_fma_f32 v[56:57], v[0:1], v[34:35], v[56:57]
	buffer_load_dwordx4 v[34:37], v25, s[0:3], s5 offen nt
	v_add_f32_dpp v18, v18, v18 quad_perm:[2,3,0,1] row_mask:0xf bank_mask:0xf bound_ctrl:1
	s_waitcnt vmcnt(7)
	v_pk_fma_f32 v[22:23], v[14:15], v[22:23], v[54:55]
	v_pk_fma_f32 v[20:21], v[12:13], v[20:21], v[56:57]
	s_waitcnt vmcnt(6)
	v_pk_fma_f32 v[60:61], v[10:11], v[48:49], v[22:23]
	v_pk_fma_f32 v[22:23], v[8:9], v[46:47], v[20:21]
	s_waitcnt vmcnt(4)
	v_pk_mul_f32 v[54:55], v[4:5], v[50:51]
	v_pk_mul_f32 v[20:21], v[6:7], v[52:53]
	v_pk_fma_f32 v[38:39], v[0:1], v[38:39], v[54:55]
	buffer_load_dwordx4 v[46:49], v25, s[0:3], s5 offen offset:2048 nt
	buffer_load_dwordx4 v[50:53], v25, s[0:3], s5 offen offset:3072 nt
	v_pk_fma_f32 v[20:21], v[2:3], v[40:41], v[20:21]
	v_add_f32_e32 v23, v22, v23
	v_add_f32_dpp v18, v18, v18 row_ror:4 row_mask:0xf bank_mask:0xf bound_ctrl:1
	s_waitcnt vmcnt(5)
	v_pk_fma_f32 v[26:27], v[12:13], v[26:27], v[38:39]
	buffer_load_dwordx4 v[38:41], v25, s[0:3], s4 offen nt
	buffer_load_dwordx4 v[54:57], v25, s[0:3], s4 offen offset:1024 nt
	v_pk_fma_f32 v[20:21], v[14:15], v[28:29], v[20:21]
	s_waitcnt vmcnt(6)
	v_pk_fma_f32 v[30:31], v[8:9], v[30:31], v[26:27]
	v_pk_fma_f32 v[62:63], v[10:11], v[32:33], v[20:21]
	v_add_f32_dpp v18, v18, v18 row_ror:8 row_mask:0xf bank_mask:0xf bound_ctrl:1
	s_waitcnt vmcnt(5)
	v_pk_mul_f32 v[20:21], v[6:7], v[44:45]
	v_pk_mul_f32 v[26:27], v[4:5], v[42:43]
	buffer_load_dwordx4 v[42:45], v25, s[0:3], s4 offen offset:2048 nt
	s_waitcnt vmcnt(5)
	v_pk_fma_f32 v[64:65], v[0:1], v[34:35], v[26:27]
	buffer_load_dwordx4 v[32:35], v25, s[0:3], s4 offen offset:3072 nt
	v_add_f32_e32 v27, v60, v61
	v_add_f32_e32 v23, v23, v27
	v_pk_fma_f32 v[36:37], v[2:3], v[36:37], v[20:21]
	v_add_f32_e32 v20, v58, v59
	v_add_f32_dpp v23, v23, v23 quad_perm:[1,0,3,2] row_mask:0xf bank_mask:0xf bound_ctrl:1
	v_add_f32_e32 v20, v66, v20
	v_mov_b32_e32 v19, v18
	v_add_f32_dpp v23, v23, v23 quad_perm:[2,3,0,1] row_mask:0xf bank_mask:0xf bound_ctrl:1
	v_add_f32_dpp v20, v20, v20 quad_perm:[1,0,3,2] row_mask:0xf bank_mask:0xf bound_ctrl:1
	v_permlane16_swap_b32_e32 v18, v19
	v_add_f32_dpp v23, v23, v23 row_ror:4 row_mask:0xf bank_mask:0xf bound_ctrl:1
	v_add_f32_dpp v20, v20, v20 quad_perm:[2,3,0,1] row_mask:0xf bank_mask:0xf bound_ctrl:1
	v_add_f32_e32 v18, v18, v19
	v_add_f32_dpp v23, v23, v23 row_ror:8 row_mask:0xf bank_mask:0xf bound_ctrl:1
	v_mov_b32_e32 v27, v23
	s_nop 1
	v_permlane16_swap_b32_e32 v23, v27
	v_add_f32_e32 v28, v23, v27
	v_add_f32_e32 v23, v30, v31
	s_waitcnt vmcnt(5)
	v_pk_fma_f32 v[30:31], v[14:15], v[48:49], v[36:37]
	v_pk_fma_f32 v[36:37], v[12:13], v[46:47], v[64:65]
	s_waitcnt vmcnt(4)
	v_pk_fma_f32 v[30:31], v[10:11], v[52:53], v[30:31]
	v_pk_fma_f32 v[36:37], v[8:9], v[50:51], v[36:37]
	v_add_f32_e32 v27, v62, v63
	v_add_f32_e32 v36, v36, v37
	v_add_f32_e32 v30, v30, v31
	v_add_f32_e32 v23, v23, v27
	v_add_f32_e32 v30, v36, v30
	v_add_f32_dpp v20, v20, v20 row_ror:4 row_mask:0xf bank_mask:0xf bound_ctrl:1
	v_add_f32_dpp v23, v23, v23 quad_perm:[1,0,3,2] row_mask:0xf bank_mask:0xf bound_ctrl:1
	v_add_f32_dpp v30, v30, v30 quad_perm:[1,0,3,2] row_mask:0xf bank_mask:0xf bound_ctrl:1
	v_add_f32_dpp v20, v20, v20 row_ror:8 row_mask:0xf bank_mask:0xf bound_ctrl:1
	v_add_f32_dpp v23, v23, v23 quad_perm:[2,3,0,1] row_mask:0xf bank_mask:0xf bound_ctrl:1
	v_add_f32_dpp v30, v30, v30 quad_perm:[2,3,0,1] row_mask:0xf bank_mask:0xf bound_ctrl:1
	v_mov_b32_e32 v21, v20
	v_add_f32_dpp v23, v23, v23 row_ror:4 row_mask:0xf bank_mask:0xf bound_ctrl:1
	v_add_f32_dpp v30, v30, v30 row_ror:4 row_mask:0xf bank_mask:0xf bound_ctrl:1
	v_permlane16_swap_b32_e32 v20, v21
	v_add_f32_dpp v23, v23, v23 row_ror:8 row_mask:0xf bank_mask:0xf bound_ctrl:1
	v_add_f32_dpp v30, v30, v30 row_ror:8 row_mask:0xf bank_mask:0xf bound_ctrl:1
	v_mov_b32_e32 v27, v23
	v_mov_b32_e32 v31, v30
	s_nop 0
	v_permlane16_swap_b32_e32 v23, v27
	v_permlane16_swap_b32_e32 v30, v31
	v_add_f32_e32 v21, v20, v21
	v_add_f32_e32 v23, v23, v27
	v_add_f32_e32 v30, v30, v31
	v_mov_b32_e32 v19, v16
	v_mov_b32_e32 v20, v17
	v_mov_b32_e32 v22, v18
	v_mov_b32_e32 v26, v21
	v_mov_b32_e32 v29, v28
	v_mov_b32_e32 v27, v23
	v_mov_b32_e32 v31, v30
	v_permlane32_swap_b32_e32 v16, v19
	v_permlane32_swap_b32_e32 v17, v20
	v_permlane32_swap_b32_e32 v18, v22
	v_permlane32_swap_b32_e32 v21, v26
	v_permlane32_swap_b32_e32 v28, v29
	v_permlane32_swap_b32_e32 v23, v27
	s_waitcnt vmcnt(2)
	v_pk_mul_f32 v[6:7], v[6:7], v[56:57]
	v_pk_mul_f32 v[4:5], v[4:5], v[54:55]
	v_pk_fma_f32 v[2:3], v[2:3], v[40:41], v[6:7]
	v_pk_fma_f32 v[0:1], v[0:1], v[38:39], v[4:5]
	v_permlane32_swap_b32_e32 v30, v31
	s_waitcnt vmcnt(1)
	v_pk_fma_f32 v[2:3], v[14:15], v[44:45], v[2:3]
	v_pk_fma_f32 v[0:1], v[12:13], v[42:43], v[0:1]
	s_waitcnt vmcnt(0)
	v_pk_fma_f32 v[2:3], v[10:11], v[34:35], v[2:3]
	v_pk_fma_f32 v[0:1], v[8:9], v[32:33], v[0:1]
	s_nop 0
	v_add_f32_e32 v0, v0, v1
	v_add_f32_e32 v1, v2, v3
	v_add_f32_e32 v0, v0, v1
	s_nop 1
	v_add_f32_dpp v0, v0, v0 quad_perm:[1,0,3,2] row_mask:0xf bank_mask:0xf bound_ctrl:1
	s_nop 1
	v_add_f32_dpp v0, v0, v0 quad_perm:[2,3,0,1] row_mask:0xf bank_mask:0xf bound_ctrl:1
	s_nop 1
	v_add_f32_dpp v0, v0, v0 row_ror:4 row_mask:0xf bank_mask:0xf bound_ctrl:1
	s_nop 1
	v_add_f32_dpp v0, v0, v0 row_ror:8 row_mask:0xf bank_mask:0xf bound_ctrl:1
	v_mov_b32_e32 v1, v0
	s_nop 1
	v_permlane16_swap_b32_e32 v0, v1
	v_add_f32_e32 v0, v0, v1
	v_mov_b32_e32 v1, v0
	s_nop 1
	v_permlane32_swap_b32_e32 v0, v1
	s_and_saveexec_b64 s[0:1], vcc
	s_cbranch_execz .LBB1_4
	v_add_f32_e32 v6, v16, v19
	v_cmp_eq_u32_e32 vcc, 0, v24
	v_add_f32_e32 v5, v17, v20
	v_add_f32_e32 v4, v18, v22
	v_cndmask_b32_e32 v6, 0, v6, vcc
	v_cmp_eq_u32_e32 vcc, 1, v24
	v_add_f32_e32 v3, v21, v26
	v_add_f32_e32 v2, v28, v29
	v_cndmask_b32_e32 v5, v6, v5, vcc
	v_cmp_eq_u32_e32 vcc, 2, v24
	v_add_f32_e32 v0, v0, v1
	v_add_f32_e32 v1, v30, v31
	v_cndmask_b32_e32 v4, v5, v4, vcc
	v_cmp_eq_u32_e32 vcc, 3, v24
	s_lshl_b32 s0, s8, 13
	s_and_b32 s0, s0, 0x1e000
	v_cndmask_b32_e32 v3, v4, v3, vcc
	v_cmp_eq_u32_e32 vcc, 4, v24
	s_add_u32 s0, s6, s0
	s_addc_u32 s1, s7, 0
	v_cndmask_b32_e32 v2, v3, v2, vcc
	v_add_f32_e32 v3, v23, v27
	v_cmp_eq_u32_e32 vcc, 5, v24
	s_nop 1
	v_cndmask_b32_e32 v2, v2, v3, vcc
	v_cmp_eq_u32_e32 vcc, 6, v24
	s_nop 1
	v_cndmask_b32_e32 v1, v2, v1, vcc
	v_cmp_eq_u32_e32 vcc, 7, v24
	s_nop 1
	v_cndmask_b32_e32 v2, v1, v0, vcc
	v_add_u32_e32 v0, s9, v25
	v_ashrrev_i32_e32 v0, 4, v0
	v_ashrrev_i32_e32 v1, 31, v0
	v_lshl_add_u64 v[0:1], v[0:1], 2, s[0:1]
	v_add_co_u32_e32 v0, vcc, 0x6000, v0
	s_nop 1
	v_addc_co_u32_e32 v1, vcc, 0, v1, vcc
	global_store_dword v[0:1], v2, off offset:64

	.amdhsa_kernel _Z13stream_kernelPKfPf
		.amdhsa_group_segment_fixed_size 4096
		.amdhsa_private_segment_fixed_size 0
		.amdhsa_kernarg_size 16
		.amdhsa_user_sgpr_count 2
		.amdhsa_user_sgpr_dispatch_ptr 0
		.amdhsa_user_sgpr_queue_ptr 0
		.amdhsa_user_sgpr_kernarg_segment_ptr 1
		.amdhsa_user_sgpr_dispatch_id 0
		.amdhsa_user_sgpr_kernarg_preload_length 0
		.amdhsa_user_sgpr_kernarg_preload_offset 0
		.amdhsa_user_sgpr_private_segment_size 0
		.amdhsa_uses_dynamic_stack 0
		.amdhsa_enable_private_segment 0
		.amdhsa_system_sgpr_workgroup_id_x 1
		.amdhsa_system_sgpr_workgroup_id_y 0
		.amdhsa_system_sgpr_workgroup_id_z 0
		.amdhsa_system_sgpr_workgroup_info 0
		.amdhsa_system_vgpr_workitem_id 0
		.amdhsa_next_free_vgpr 67
		.amdhsa_next_free_sgpr 13
		.amdhsa_accum_offset 68
		.amdhsa_reserve_vcc 1
		.amdhsa_float_round_mode_32 0
		.amdhsa_float_round_mode_16_64 0
		.amdhsa_float_denorm_mode_32 3
		.amdhsa_float_denorm_mode_16_64 3
		.amdhsa_dx10_clamp 1
		.amdhsa_ieee_mode 1
		.amdhsa_fp16_overflow 0
		.amdhsa_tg_split 0
		.amdhsa_exception_fp_ieee_invalid_op 0
		.amdhsa_exception_fp_denorm_src 0
		.amdhsa_exception_fp_ieee_div_zero 0
		.amdhsa_exception_fp_ieee_overflow 0
		.amdhsa_exception_fp_ieee_underflow 0
		.amdhsa_exception_fp_ieee_inexact 0
		.amdhsa_exception_int_div_zero 0
	.end_amdhsa_kernel

.Lfunc_end1:
	.size	_Z13stream_kernelPKfPf, .Lfunc_end1-_Z13stream_kernelPKfPf
	.set _Z13stream_kernelPKfPf.num_vgpr, 67
	.set _Z13stream_kernelPKfPf.num_agpr, 0
	.set _Z13stream_kernelPKfPf.numbered_sgpr, 13
	.set _Z13stream_kernelPKfPf.num_named_barrier, 0
	.set _Z13stream_kernelPKfPf.private_seg_size, 0
	.set _Z13stream_kernelPKfPf.uses_vcc, 1
	.set _Z13stream_kernelPKfPf.uses_flat_scratch, 0
	.set _Z13stream_kernelPKfPf.has_dyn_sized_stack, 0
	.set _Z13stream_kernelPKfPf.has_recursion, 0
	.set _Z13stream_kernelPKfPf.has_indirect_call, 0

amdhsa.kernels:
  - .agpr_count:     0
    .args:
      - .actual_access:  read_only
        .address_space:  global
        .offset:         0
        .size:           8
        .value_kind:     global_buffer
      - .actual_access:  read_only
        .address_space:  global
        .offset:         8
        .size:           8
        .value_kind:     global_buffer
      - .actual_access:  read_only
        .address_space:  global
        .offset:         16
        .size:           8
        .value_kind:     global_buffer
      - .actual_access:  read_only
        .address_space:  global
        .offset:         24
        .size:           8
        .value_kind:     global_buffer
      - .actual_access:  write_only
        .address_space:  global
        .offset:         32
        .size:           8
        .value_kind:     global_buffer
    .group_segment_fixed_size: 2112
    .kernarg_segment_align: 8
    .kernarg_segment_size: 40
    .language:       OpenCL C
    .language_version:
      - 2
      - 0
    .max_flat_workgroup_size: 1024
    .name:           _Z11prep_kernelPKfS0_S0_S0_Pf
    .private_segment_fixed_size: 0
    .sgpr_count:     34
    .sgpr_spill_count: 0
    .symbol:         _Z11prep_kernelPKfS0_S0_S0_Pf.kd
    .uniform_work_group_size: 1
    .uses_dynamic_stack: false
    .vgpr_count:     72
    .vgpr_spill_count: 0
    .wavefront_size: 64
  - .agpr_count:     0
    .args:
      - .actual_access:  read_only
        .address_space:  global
        .offset:         0
        .size:           8
        .value_kind:     global_buffer
      - .address_space:  global
        .offset:         8
        .size:           8
        .value_kind:     global_buffer
    .group_segment_fixed_size: 4096
    .kernarg_segment_align: 8
    .kernarg_segment_size: 16
    .language:       OpenCL C
    .language_version:
      - 2
      - 0
    .max_flat_workgroup_size: 1024
    .name:           _Z13stream_kernelPKfPf
    .private_segment_fixed_size: 0
    .sgpr_count:     19
    .sgpr_spill_count: 0
    .symbol:         _Z13stream_kernelPKfPf.kd
    .uniform_work_group_size: 1
    .uses_dynamic_stack: false
    .vgpr_count:     67
    .vgpr_spill_count: 0
    .wavefront_size: 64
  - .agpr_count:     0
    .args:
      - .actual_access:  read_only
        .address_space:  global
        .offset:         0
        .size:           8
        .value_kind:     global_buffer
      - .actual_access:  write_only
        .address_space:  global
        .offset:         8
        .size:           8
        .value_kind:     global_buffer
    .group_segment_fixed_size: 32
    .kernarg_segment_align: 8
    .kernarg_segment_size: 16
    .language:       OpenCL C
    .language_version:
      - 2
      - 0
    .max_flat_workgroup_size: 256
    .name:           _Z14softmax_kernelPKfPf
    .private_segment_fixed_size: 0
    .sgpr_count:     26
    .sgpr_spill_count: 0
    .symbol:         _Z14softmax_kernelPKfPf.kd
    .uniform_work_group_size: 1
    .uses_dynamic_stack: false
    .vgpr_count:     32
    .vgpr_spill_count: 0
    .wavefront_size: 64
